# speedup vs baseline: 1.0597x; 1.0019x over previous
.Lep_pn0:
	v_pk_fma_f32 v[78:79], v[78:79], v[240:241], v[34:35]
	v_pk_fma_f32 v[80:81], v[80:81], v[240:241], v[36:37]
	v_max_f32_e32 v78, 0, v78
	v_max_f32_e32 v79, 0, v79
	v_max_f32_e32 v80, 0, v80
	v_max_f32_e32 v81, 0, v81
	v_cvt_pk_f16_f32 v246, v78, v79
	v_cvt_pk_f16_f32 v247, v80, v81
	v_pk_fma_f32 v[74:75], v[74:75], v[240:241], v[26:27]
	v_pk_fma_f32 v[76:77], v[76:77], v[240:241], v[28:29]
	v_max_f32_e32 v74, 0, v74
	v_max_f32_e32 v75, 0, v75
	v_max_f32_e32 v76, 0, v76
	v_max_f32_e32 v77, 0, v77
	v_cvt_pk_f16_f32 v248, v74, v75
	v_cvt_pk_f16_f32 v249, v76, v77
	s_add_u32 s96, s28, 0x0
	s_addc_u32 s97, s29, 0
	v_permlane16_swap_b32_e32 v246, v248
	v_permlane16_swap_b32_e32 v247, v249
	global_store_dwordx4 v238, v[246:249], s[96:97] sc1
	v_pk_fma_f32 v[70:71], v[70:71], v[240:241], v[18:19]
	v_pk_fma_f32 v[72:73], v[72:73], v[240:241], v[20:21]
	v_max_f32_e32 v70, 0, v70
	v_max_f32_e32 v71, 0, v71
	v_max_f32_e32 v72, 0, v72
	v_max_f32_e32 v73, 0, v73
	v_cvt_pk_f16_f32 v250, v70, v71
	v_cvt_pk_f16_f32 v251, v72, v73
	v_pk_fma_f32 v[66:67], v[66:67], v[240:241], v[10:11]
	v_pk_fma_f32 v[68:69], v[68:69], v[240:241], v[12:13]
	v_max_f32_e32 v66, 0, v66
	v_max_f32_e32 v67, 0, v67
	v_max_f32_e32 v68, 0, v68
	v_max_f32_e32 v69, 0, v69
	v_cvt_pk_f16_f32 v252, v66, v67
	v_cvt_pk_f16_f32 v253, v68, v69
	s_add_u32 s96, s28, 0x1000
	s_addc_u32 s97, s29, 0
	v_permlane16_swap_b32_e32 v250, v252
	v_permlane16_swap_b32_e32 v251, v253
	global_store_dwordx4 v238, v[250:253], s[96:97] sc1
	v_pk_fma_f32 v[62:63], v[62:63], v[240:241], v[34:35]
	v_pk_fma_f32 v[64:65], v[64:65], v[240:241], v[36:37]
	v_max_f32_e32 v62, 0, v62
	v_max_f32_e32 v63, 0, v63
	v_max_f32_e32 v64, 0, v64
	v_max_f32_e32 v65, 0, v65
	v_cvt_pk_f16_f32 v246, v62, v63
	v_cvt_pk_f16_f32 v247, v64, v65
	v_pk_fma_f32 v[58:59], v[58:59], v[240:241], v[26:27]
	v_pk_fma_f32 v[60:61], v[60:61], v[240:241], v[28:29]
	v_max_f32_e32 v58, 0, v58
	v_max_f32_e32 v59, 0, v59
	v_max_f32_e32 v60, 0, v60
	v_max_f32_e32 v61, 0, v61
	v_cvt_pk_f16_f32 v248, v58, v59
	v_cvt_pk_f16_f32 v249, v60, v61
	s_add_u32 s96, s28, 0x2000
	s_addc_u32 s97, s29, 0
	v_permlane16_swap_b32_e32 v246, v248
	v_permlane16_swap_b32_e32 v247, v249
	global_store_dwordx4 v238, v[246:249], s[96:97] sc1
	v_pk_fma_f32 v[54:55], v[54:55], v[240:241], v[18:19]
	v_pk_fma_f32 v[56:57], v[56:57], v[240:241], v[20:21]
	v_max_f32_e32 v54, 0, v54
	v_max_f32_e32 v55, 0, v55
	v_max_f32_e32 v56, 0, v56
	v_max_f32_e32 v57, 0, v57
	v_cvt_pk_f16_f32 v250, v54, v55
	v_cvt_pk_f16_f32 v251, v56, v57
	v_pk_fma_f32 v[50:51], v[50:51], v[240:241], v[10:11]
	v_pk_fma_f32 v[52:53], v[52:53], v[240:241], v[12:13]
	v_max_f32_e32 v50, 0, v50
	v_max_f32_e32 v51, 0, v51
	v_max_f32_e32 v52, 0, v52
	v_max_f32_e32 v53, 0, v53
	v_cvt_pk_f16_f32 v252, v50, v51
	v_cvt_pk_f16_f32 v253, v52, v53
	s_add_u32 s96, s28, 0x3000
	s_addc_u32 s97, s29, 0
	v_permlane16_swap_b32_e32 v250, v252
	v_permlane16_swap_b32_e32 v251, v253
	global_store_dwordx4 v238, v[250:253], s[96:97] sc1
	v_pk_fma_f32 v[46:47], v[46:47], v[240:241], v[34:35]
	v_pk_fma_f32 v[48:49], v[48:49], v[240:241], v[36:37]
	v_max_f32_e32 v46, 0, v46
	v_max_f32_e32 v47, 0, v47
	v_max_f32_e32 v48, 0, v48
	v_max_f32_e32 v49, 0, v49
	v_cvt_pk_f16_f32 v246, v46, v47
	v_cvt_pk_f16_f32 v247, v48, v49
	v_pk_fma_f32 v[42:43], v[42:43], v[240:241], v[26:27]
	v_pk_fma_f32 v[44:45], v[44:45], v[240:241], v[28:29]
	v_max_f32_e32 v42, 0, v42
	v_max_f32_e32 v43, 0, v43
	v_max_f32_e32 v44, 0, v44
	v_max_f32_e32 v45, 0, v45
	v_cvt_pk_f16_f32 v248, v42, v43
	v_cvt_pk_f16_f32 v249, v44, v45
	s_add_u32 s96, s28, 0x4000
	s_addc_u32 s97, s29, 0
	v_permlane16_swap_b32_e32 v246, v248
	v_permlane16_swap_b32_e32 v247, v249
	global_store_dwordx4 v238, v[246:249], s[96:97] sc1
	v_pk_fma_f32 v[38:39], v[38:39], v[240:241], v[18:19]
	v_pk_fma_f32 v[40:41], v[40:41], v[240:241], v[20:21]
	v_max_f32_e32 v38, 0, v38
	v_max_f32_e32 v39, 0, v39
	v_max_f32_e32 v40, 0, v40
	v_max_f32_e32 v41, 0, v41
	v_cvt_pk_f16_f32 v250, v38, v39
	v_cvt_pk_f16_f32 v251, v40, v41
	v_pk_fma_f32 v[30:31], v[30:31], v[240:241], v[10:11]
	v_pk_fma_f32 v[32:33], v[32:33], v[240:241], v[12:13]
	v_max_f32_e32 v30, 0, v30
	v_max_f32_e32 v31, 0, v31
	v_max_f32_e32 v32, 0, v32
	v_max_f32_e32 v33, 0, v33
	v_cvt_pk_f16_f32 v252, v30, v31
	v_cvt_pk_f16_f32 v253, v32, v33
	s_add_u32 s96, s28, 0x5000
	s_addc_u32 s97, s29, 0
	v_permlane16_swap_b32_e32 v250, v252
	v_permlane16_swap_b32_e32 v251, v253
	global_store_dwordx4 v238, v[250:253], s[96:97] sc1
	v_pk_fma_f32 v[22:23], v[22:23], v[240:241], v[34:35]
	v_pk_fma_f32 v[24:25], v[24:25], v[240:241], v[36:37]
	v_max_f32_e32 v22, 0, v22
	v_max_f32_e32 v23, 0, v23
	v_max_f32_e32 v24, 0, v24
	v_max_f32_e32 v25, 0, v25
	v_cvt_pk_f16_f32 v246, v22, v23
	v_cvt_pk_f16_f32 v247, v24, v25
	v_pk_fma_f32 v[14:15], v[14:15], v[240:241], v[26:27]
	v_pk_fma_f32 v[16:17], v[16:17], v[240:241], v[28:29]
	v_max_f32_e32 v14, 0, v14
	v_max_f32_e32 v15, 0, v15
	v_max_f32_e32 v16, 0, v16
	v_max_f32_e32 v17, 0, v17
	v_cvt_pk_f16_f32 v248, v14, v15
	v_cvt_pk_f16_f32 v249, v16, v17
	s_add_u32 s96, s28, 0x6000
	s_addc_u32 s97, s29, 0
	v_permlane16_swap_b32_e32 v246, v248
	v_permlane16_swap_b32_e32 v247, v249
	global_store_dwordx4 v238, v[246:249], s[96:97] sc1
	v_pk_fma_f32 v[6:7], v[6:7], v[240:241], v[18:19]
	v_pk_fma_f32 v[8:9], v[8:9], v[240:241], v[20:21]
	v_max_f32_e32 v6, 0, v6
	v_max_f32_e32 v7, 0, v7
	v_max_f32_e32 v8, 0, v8
	v_max_f32_e32 v9, 0, v9
	v_cvt_pk_f16_f32 v250, v6, v7
	v_cvt_pk_f16_f32 v251, v8, v9
	v_pk_fma_f32 v[2:3], v[2:3], v[240:241], v[10:11]
	v_pk_fma_f32 v[4:5], v[4:5], v[240:241], v[12:13]
	v_max_f32_e32 v2, 0, v2
	v_max_f32_e32 v3, 0, v3
	v_max_f32_e32 v4, 0, v4
	v_max_f32_e32 v5, 0, v5
	v_cvt_pk_f16_f32 v252, v2, v3
	v_cvt_pk_f16_f32 v253, v4, v5
	s_add_u32 s96, s28, 0x7000
	s_addc_u32 s97, s29, 0
	v_permlane16_swap_b32_e32 v250, v252
	v_permlane16_swap_b32_e32 v251, v253
	global_store_dwordx4 v238, v[250:253], s[96:97] sc1
	v_pk_fma_f32 v[142:143], v[142:143], v[240:241], v[34:35]
	v_pk_fma_f32 v[144:145], v[144:145], v[240:241], v[36:37]
	v_max_f32_e32 v142, 0, v142
	v_max_f32_e32 v143, 0, v143
	v_max_f32_e32 v144, 0, v144
	v_max_f32_e32 v145, 0, v145
	v_cvt_pk_f16_f32 v242, v142, v143
	v_cvt_pk_f16_f32 v243, v144, v145
	ds_write_b64 v236, v[242:243] offset:0
	v_pk_fma_f32 v[138:139], v[138:139], v[240:241], v[26:27]
	v_pk_fma_f32 v[140:141], v[140:141], v[240:241], v[28:29]
	v_max_f32_e32 v138, 0, v138
	v_max_f32_e32 v139, 0, v139
	v_max_f32_e32 v140, 0, v140
	v_max_f32_e32 v141, 0, v141
	v_cvt_pk_f16_f32 v244, v138, v139
	v_cvt_pk_f16_f32 v245, v140, v141
	ds_write_b64 v237, v[244:245] offset:0
	v_pk_fma_f32 v[134:135], v[134:135], v[240:241], v[18:19]
	v_pk_fma_f32 v[136:137], v[136:137], v[240:241], v[20:21]
	v_max_f32_e32 v134, 0, v134
	v_max_f32_e32 v135, 0, v135
	v_max_f32_e32 v136, 0, v136
	v_max_f32_e32 v137, 0, v137
	v_cvt_pk_f16_f32 v242, v134, v135
	v_cvt_pk_f16_f32 v243, v136, v137
	ds_write_b64 v236, v[242:243] offset:4096
	v_pk_fma_f32 v[130:131], v[130:131], v[240:241], v[10:11]
	v_pk_fma_f32 v[132:133], v[132:133], v[240:241], v[12:13]
	v_max_f32_e32 v130, 0, v130
	v_max_f32_e32 v131, 0, v131
	v_max_f32_e32 v132, 0, v132
	v_max_f32_e32 v133, 0, v133
	v_cvt_pk_f16_f32 v244, v130, v131
	v_cvt_pk_f16_f32 v245, v132, v133
	ds_write_b64 v237, v[244:245] offset:4096
	v_pk_fma_f32 v[126:127], v[126:127], v[240:241], v[34:35]
	v_pk_fma_f32 v[128:129], v[128:129], v[240:241], v[36:37]
	v_max_f32_e32 v126, 0, v126
	v_max_f32_e32 v127, 0, v127
	v_max_f32_e32 v128, 0, v128
	v_max_f32_e32 v129, 0, v129
	v_cvt_pk_f16_f32 v242, v126, v127
	v_cvt_pk_f16_f32 v243, v128, v129
	ds_write_b64 v236, v[242:243] offset:16384
	v_pk_fma_f32 v[122:123], v[122:123], v[240:241], v[26:27]
	v_pk_fma_f32 v[124:125], v[124:125], v[240:241], v[28:29]
	v_max_f32_e32 v122, 0, v122
	v_max_f32_e32 v123, 0, v123
	v_max_f32_e32 v124, 0, v124
	v_max_f32_e32 v125, 0, v125
	v_cvt_pk_f16_f32 v244, v122, v123
	v_cvt_pk_f16_f32 v245, v124, v125
	ds_write_b64 v237, v[244:245] offset:16384
	v_pk_fma_f32 v[118:119], v[118:119], v[240:241], v[18:19]
	v_pk_fma_f32 v[120:121], v[120:121], v[240:241], v[20:21]
	v_max_f32_e32 v118, 0, v118
	v_max_f32_e32 v119, 0, v119
	v_max_f32_e32 v120, 0, v120
	v_max_f32_e32 v121, 0, v121
	v_cvt_pk_f16_f32 v242, v118, v119
	v_cvt_pk_f16_f32 v243, v120, v121
	ds_write_b64 v236, v[242:243] offset:20480
	v_pk_fma_f32 v[114:115], v[114:115], v[240:241], v[10:11]
	v_pk_fma_f32 v[116:117], v[116:117], v[240:241], v[12:13]
	v_max_f32_e32 v114, 0, v114
	v_max_f32_e32 v115, 0, v115
	v_max_f32_e32 v116, 0, v116
	v_max_f32_e32 v117, 0, v117
	v_cvt_pk_f16_f32 v244, v114, v115
	v_cvt_pk_f16_f32 v245, v116, v117
	ds_write_b64 v237, v[244:245] offset:20480
	v_pk_fma_f32 v[110:111], v[110:111], v[240:241], v[34:35]
	v_pk_fma_f32 v[112:113], v[112:113], v[240:241], v[36:37]
	v_max_f32_e32 v110, 0, v110
	v_max_f32_e32 v111, 0, v111
	v_max_f32_e32 v112, 0, v112
	v_max_f32_e32 v113, 0, v113
	v_cvt_pk_f16_f32 v242, v110, v111
	v_cvt_pk_f16_f32 v243, v112, v113
	ds_write_b64 v236, v[242:243] offset:32768
	v_pk_fma_f32 v[106:107], v[106:107], v[240:241], v[26:27]
	v_pk_fma_f32 v[108:109], v[108:109], v[240:241], v[28:29]
	v_max_f32_e32 v106, 0, v106
	v_max_f32_e32 v107, 0, v107
	v_max_f32_e32 v108, 0, v108
	v_max_f32_e32 v109, 0, v109
	v_cvt_pk_f16_f32 v244, v106, v107
	v_cvt_pk_f16_f32 v245, v108, v109
	ds_write_b64 v237, v[244:245] offset:32768
	v_pk_fma_f32 v[102:103], v[102:103], v[240:241], v[18:19]
	v_pk_fma_f32 v[104:105], v[104:105], v[240:241], v[20:21]
	v_max_f32_e32 v102, 0, v102
	v_max_f32_e32 v103, 0, v103
	v_max_f32_e32 v104, 0, v104
	v_max_f32_e32 v105, 0, v105
	v_cvt_pk_f16_f32 v242, v102, v103
	v_cvt_pk_f16_f32 v243, v104, v105
	ds_write_b64 v236, v[242:243] offset:36864
	v_pk_fma_f32 v[98:99], v[98:99], v[240:241], v[10:11]
	v_pk_fma_f32 v[100:101], v[100:101], v[240:241], v[12:13]
	v_max_f32_e32 v98, 0, v98
	v_max_f32_e32 v99, 0, v99
	v_max_f32_e32 v100, 0, v100
	v_max_f32_e32 v101, 0, v101
	v_cvt_pk_f16_f32 v244, v98, v99
	v_cvt_pk_f16_f32 v245, v100, v101
	ds_write_b64 v237, v[244:245] offset:36864
	v_pk_fma_f32 v[94:95], v[94:95], v[240:241], v[34:35]
	v_pk_fma_f32 v[96:97], v[96:97], v[240:241], v[36:37]
	v_max_f32_e32 v94, 0, v94
	v_max_f32_e32 v95, 0, v95
	v_max_f32_e32 v96, 0, v96
	v_max_f32_e32 v97, 0, v97
	v_cvt_pk_f16_f32 v242, v94, v95
	v_cvt_pk_f16_f32 v243, v96, v97
	ds_write_b64 v236, v[242:243] offset:49152
	v_pk_fma_f32 v[90:91], v[90:91], v[240:241], v[26:27]
	v_pk_fma_f32 v[92:93], v[92:93], v[240:241], v[28:29]
	v_max_f32_e32 v90, 0, v90
	v_max_f32_e32 v91, 0, v91
	v_max_f32_e32 v92, 0, v92
	v_max_f32_e32 v93, 0, v93
	v_cvt_pk_f16_f32 v244, v90, v91
	v_cvt_pk_f16_f32 v245, v92, v93
	ds_write_b64 v237, v[244:245] offset:49152
	v_pk_fma_f32 v[86:87], v[86:87], v[240:241], v[18:19]
	v_pk_fma_f32 v[88:89], v[88:89], v[240:241], v[20:21]
	v_max_f32_e32 v86, 0, v86
	v_max_f32_e32 v87, 0, v87
	v_max_f32_e32 v88, 0, v88
	v_max_f32_e32 v89, 0, v89
	v_cvt_pk_f16_f32 v242, v86, v87
	v_cvt_pk_f16_f32 v243, v88, v89
	ds_write_b64 v236, v[242:243] offset:53248
	v_pk_fma_f32 v[82:83], v[82:83], v[240:241], v[10:11]
	v_pk_fma_f32 v[84:85], v[84:85], v[240:241], v[12:13]
	v_max_f32_e32 v82, 0, v82
	v_max_f32_e32 v83, 0, v83
	v_max_f32_e32 v84, 0, v84
	v_max_f32_e32 v85, 0, v85
	v_cvt_pk_f16_f32 v244, v82, v83
	v_cvt_pk_f16_f32 v245, v84, v85
	ds_write_b64 v237, v[244:245] offset:53248
